# FoX attention tile: forget-bias subtraction as 16 packed adds (neg modifiers) instead of 32 scalar subs
# baseline (speedup 1.0000x reference)
.LBB0_415:
	s_add_i32 s14, s65, 0x42
	s_min_u32 s14, s14, s40
	s_mul_i32 s52, s14, 0xc0000
	s_mul_hi_u32 s53, s14, 0xc0000
	s_add_u32 s48, s0, s52
	s_mul_i32 s67, s66, 0x8800
	s_addc_u32 s49, s1, s53
	s_add_i32 s54, s67, 0xffff7800
	s_cmp_gt_i32 s66, 0
	s_cselect_b32 s54, s54, 0x11000
	s_add_i32 s54, s54, 0
	s_add_u32 s52, s2, s52
	s_addc_u32 s53, s3, s53
	s_add_i32 s55, s54, s59
	s_waitcnt vmcnt(5) lgkmcnt(0)
	s_barrier
	v_lshl_add_u64 v[106:107], s[48:49], 0, v[146:147]
	s_mov_b32 m0, s55
	s_lshl_b32 s14, s14, 6
	global_load_lds_dwordx4 v[106:107], off
	v_lshl_add_u64 v[106:107], s[52:53], 0, v[148:149]
	s_add_i32 m0, s55, 0x4000
	s_nop 0
	global_load_lds_dwordx4 v[106:107], off
	v_lshl_add_u64 v[106:107], s[48:49], 0, v[152:153]
	s_add_i32 s48, s54, s62
	s_mov_b32 m0, s48
	s_nop 0
	global_load_lds_dwordx4 v[106:107], off
	v_lshl_add_u64 v[106:107], s[52:53], 0, v[154:155]
	s_add_i32 m0, s48, 0x4000
	s_nop 0
	global_load_lds_dwordx4 v[106:107], off
	v_lshl_add_u64 v[106:107], s[14:15], 2, v[156:157]
	s_add_i32 s14, s54, s63
	s_add_i32 m0, s14, 0x8000
	s_cmp_gt_i32 s56, s41
	global_load_lds_dword v[106:107], off
	s_cbranch_scc1 .LBB0_414
	s_add_i32 s14, s56, 63
	s_add_i32 s52, s23, s67
	s_cmp_gt_i32 s14, s38
	v_sub_f32_e32 v160, v143, v167
	s_mov_b64 s[48:49], -1
	v_add_u32_e32 v169, s52, v159
	v_sub_f32_e32 v158, v151, v168
	s_cbranch_scc1 .LBB0_418
	ds_read_b128 v[110:113], v169 offset:32768
	ds_read_b128 v[118:121], v169 offset:32832
	ds_read_b128 v[130:133], v169 offset:32896
	ds_read_b128 v[134:137], v169 offset:32960
	s_mov_b64 s[48:49], 0
	s_waitcnt lgkmcnt(0)
	v_pk_add_f32 v[108:109], v[160:161], v[112:113] op_sel_hi:[0,1] neg_lo:[0,1] neg_hi:[0,1]
	v_pk_add_f32 v[106:107], v[160:161], v[110:111] op_sel_hi:[0,1] neg_lo:[0,1] neg_hi:[0,1]
	v_pk_add_f32 v[116:117], v[160:161], v[120:121] op_sel_hi:[0,1] neg_lo:[0,1] neg_hi:[0,1]
	v_pk_add_f32 v[114:115], v[160:161], v[118:119] op_sel_hi:[0,1] neg_lo:[0,1] neg_hi:[0,1]
	v_pk_add_f32 v[124:125], v[160:161], v[132:133] op_sel_hi:[0,1] neg_lo:[0,1] neg_hi:[0,1]
	v_pk_add_f32 v[122:123], v[160:161], v[130:131] op_sel_hi:[0,1] neg_lo:[0,1] neg_hi:[0,1]
	v_pk_add_f32 v[128:129], v[160:161], v[136:137] op_sel_hi:[0,1] neg_lo:[0,1] neg_hi:[0,1]
	v_pk_add_f32 v[126:127], v[160:161], v[134:135] op_sel_hi:[0,1] neg_lo:[0,1] neg_hi:[0,1]
	v_pk_add_f32 v[112:113], v[158:159], v[112:113] op_sel_hi:[0,1] neg_lo:[0,1] neg_hi:[0,1]
	v_pk_add_f32 v[110:111], v[158:159], v[110:111] op_sel_hi:[0,1] neg_lo:[0,1] neg_hi:[0,1]
	v_pk_add_f32 v[120:121], v[158:159], v[120:121] op_sel_hi:[0,1] neg_lo:[0,1] neg_hi:[0,1]
	v_pk_add_f32 v[118:119], v[158:159], v[118:119] op_sel_hi:[0,1] neg_lo:[0,1] neg_hi:[0,1]
	v_pk_add_f32 v[132:133], v[158:159], v[132:133] op_sel_hi:[0,1] neg_lo:[0,1] neg_hi:[0,1]
	v_pk_add_f32 v[130:131], v[158:159], v[130:131] op_sel_hi:[0,1] neg_lo:[0,1] neg_hi:[0,1]
	v_pk_add_f32 v[136:137], v[158:159], v[136:137] op_sel_hi:[0,1] neg_lo:[0,1] neg_hi:[0,1]
	v_pk_add_f32 v[134:135], v[158:159], v[134:135] op_sel_hi:[0,1] neg_lo:[0,1] neg_hi:[0,1]
